# gate/up expert weights converted inside the MLA tile loop; down projections via barrier-wait work and the pre-MoE drain only (no drains around attention)
# baseline (speedup 1.0000x reference)
; #define LAS __attribute__((address_space(3)))
; __device__ __forceinline__ unsigned xb_ld(unsigned* p)              { return __hip_atomic_load(p, __ATOMIC_RELAXED, __HIP_MEMORY_SCOPE_AGENT); }
; __device__ __forceinline__ unsigned xb_add(unsigned* p, unsigned v) { return __hip_atomic_fetch_add(p, v, __ATOMIC_RELAXED, __HIP_MEMORY_SCOPE_AGENT); }
;     __device__ __forceinline__ unsigned char* ws() const { return *(unsigned char* const __attribute__((address_space(4)))*)(p + 232); }
;     volatile LAS unsigned* st = (volatile LAS unsigned*)(lds + MISC_OFF) + 8;
;     unsigned* qw = (unsigned*)(ws + WS_CTL) + CW_Q;
;     int tl = tid_x(); asm volatile("" : "+v"(tl));
;     const int wave = __builtin_amdgcn_readfirstlane(tl >> 6), lane = tl & 63;
;     LAS float* scr = (LAS float*)(lds + wave * 16640);
;     __syncthreads();
;     unsigned ahead = 0xFFFFFFFFu;
;     if (tl == 0 && max_claims > 0) { if (xb_ld(qw) < (unsigned)target) ahead = xb_add(qw, 32u); }
; __global__ void __launch_bounds__(512, 2) mk_fwd(Args args) {
;     ...
;             const bool conv_first = ((blockIdx.x >> 3) & 1) != 0;
;             if (conv_first) conv_drain(a, ws, F.lds, (l + 1) * Q_PER_L, CONV_QUOTA);
.LBB0_690:
	v_readlane_b32 s0, v254, 2
	v_readlane_b32 s1, v254, 3
	s_and_b64 vcc, exec, s[0:1]
	s_mov_b64 s[36:37], 0x100
	s_waitcnt lgkmcnt(0)
	s_barrier
	s_branch .LBB0_782
	v_readlane_b32 s0, v254, 60
	s_mul_i32 s27, s0, 0xc300
	s_add_i32 s25, s27, 0xc300
	s_add_u32 s4, s8, 0x20000
	s_getreg_b32 s0, hwreg(HW_REG_HW_ID, 0, 6)
	s_addc_u32 s5, s9, 0
	s_and_b32 s0, s0, 63
	s_lshl_b32 s0, s0, 2
	s_add_i32 s0, s0, 0
	s_add_i32 s0, s0, 0x23f00
	v_mov_b32_e32 v0, s0
	ds_read_b32 v0, v0
	v_mbcnt_lo_u32_b32 v1, -1, 0
	v_mbcnt_hi_u32_b32 v1, -1, v1
	v_readlane_b32 s1, v254, 61
	v_mov_b32_e32 v129, -1
	s_waitcnt lgkmcnt(0)
	v_readfirstlane_b32 s0, v0
	s_nop 1
	v_lshl_add_u32 v0, s0, 6, v1
	s_nop 0
	v_readfirstlane_b32 s14, v0
	v_cmp_eq_u32_e64 s[2:3], 0, v0
	s_barrier
	s_and_saveexec_b64 s[0:1], s[2:3]
	s_cbranch_execz .LBB0_696
	global_load_dword v1, v193, s[4:5] sc1
	v_mov_b32_e32 v129, -1
	s_waitcnt vmcnt(0)
	v_cmp_le_u32_e32 vcc, s25, v1
	s_cbranch_vccnz .LBB0_696
	s_mov_b64 s[12:13], exec
	v_mbcnt_lo_u32_b32 v1, s12, 0
	v_mbcnt_hi_u32_b32 v1, s13, v1
	v_cmp_eq_u32_e32 vcc, 0, v1
	s_and_saveexec_b64 s[10:11], vcc
	s_cbranch_execz .LBB0_695
	s_bcnt1_i32_b64 s12, s[12:13]
	s_lshl_b32 s12, s12, 5
	v_mov_b32_e32 v2, s12
	global_atomic_add v2, v193, v2, s[4:5] sc0

; #define LAS __attribute__((address_space(3)))
; __device__ __forceinline__ unsigned xb_ld(unsigned* p)              { return __hip_atomic_load(p, __ATOMIC_RELAXED, __HIP_MEMORY_SCOPE_AGENT); }
; __device__ __forceinline__ unsigned xb_add(unsigned* p, unsigned v) { return __hip_atomic_fetch_add(p, v, __ATOMIC_RELAXED, __HIP_MEMORY_SCOPE_AGENT); }
;     __device__ __forceinline__ unsigned char* ws() const { return *(unsigned char* const __attribute__((address_space(4)))*)(p + 232); }
;     volatile LAS unsigned* st = (volatile LAS unsigned*)(lds + MISC_OFF) + 8;
;     unsigned* qw = (unsigned*)(ws + WS_CTL) + CW_Q;
;     int tl = tid_x(); asm volatile("" : "+v"(tl));
;     const int wave = __builtin_amdgcn_readfirstlane(tl >> 6), lane = tl & 63;
;     LAS float* scr = (LAS float*)(lds + wave * 16640);
;     __syncthreads();
;     unsigned ahead = 0xFFFFFFFFu;
;     if (tl == 0 && max_claims > 0) { if (xb_ld(qw) < (unsigned)target) ahead = xb_add(qw, 32u); }
; __global__ void __launch_bounds__(512, 2) mk_fwd(Args args) {
;     ...
;             const bool conv_first = ((blockIdx.x >> 3) & 1) != 0;
;             if (conv_first) conv_drain(a, ws, F.lds, (l + 1) * Q_PER_L, CONV_QUOTA);
;             for (int c = blockIdx.x; c < 256; c += F.G) {
;                 const int xcd = c & 7, j = c >> 3;
;                 if (ATT_MASK & 1) att::attn_unit<att::MODE_MLA>(P, (xcd * 2 + (j >> 4)) * 16 + (j & 15), al);
;             }
;             if (!conv_first) conv_drain(a, ws, F.lds, (l + 1) * Q_PER_L, CONV_QUOTA);
.LBB0_795:
	v_readlane_b32 s0, v254, 5
	v_readlane_b32 s1, v254, 6
	s_and_b64 vcc, exec, s[0:1]
	s_branch .LBB0_887
	v_readlane_b32 s0, v254, 60
	s_mul_i32 s27, s0, 0xc300
	s_add_i32 s25, s27, 0xc300
	s_add_u32 s4, s8, 0x20000
	s_getreg_b32 s0, hwreg(HW_REG_HW_ID, 0, 6)
	s_addc_u32 s5, s9, 0
	s_and_b32 s0, s0, 63
	s_lshl_b32 s0, s0, 2
	s_add_i32 s0, s0, 0
	s_add_i32 s0, s0, 0x23f00
	s_waitcnt vmcnt(15)
	v_mov_b32_e32 v0, s0
	ds_read_b32 v0, v0
	v_mbcnt_lo_u32_b32 v1, -1, 0
	v_mbcnt_hi_u32_b32 v1, -1, v1
	v_readlane_b32 s1, v254, 61
	v_mov_b32_e32 v129, -1
	s_waitcnt lgkmcnt(0)
	v_readfirstlane_b32 s0, v0
	s_nop 1
	v_lshl_add_u32 v0, s0, 6, v1
	s_nop 0
	v_readfirstlane_b32 s14, v0
	v_cmp_eq_u32_e64 s[2:3], 0, v0
	s_barrier
	s_and_saveexec_b64 s[0:1], s[2:3]
	s_cbranch_execz .LBB0_801
	global_load_dword v1, v193, s[4:5] sc1
	v_mov_b32_e32 v129, -1
	s_waitcnt vmcnt(0)
	v_cmp_le_u32_e32 vcc, s25, v1
	s_cbranch_vccnz .LBB0_801
	s_mov_b64 s[12:13], exec
	v_mbcnt_lo_u32_b32 v1, s12, 0
	v_mbcnt_hi_u32_b32 v1, s13, v1
	v_cmp_eq_u32_e32 vcc, 0, v1
	s_and_saveexec_b64 s[10:11], vcc
	s_cbranch_execz .LBB0_800
	s_bcnt1_i32_b64 s12, s[12:13]
	s_lshl_b32 s12, s12, 5
	v_mov_b32_e32 v2, s12
	global_atomic_add v2, v193, v2, s[4:5] sc0
